# ssd_states+index_scores phase: every workgroup runs index_scores before ssd_states so the following scan finds the chunk states still cached
# baseline (speedup 1.0000x reference)
.LBB0_424:
	s_andn2_b64 vcc, exec, s[0:1]
	v_readlane_b32 s0, v253, 2
	v_readlane_b32 s1, v253, 3
	s_waitcnt vmcnt(0)
	s_nop 0
	v_cndmask_b32_e64 v0, 0, 1, s[0:1]
	v_cmp_ne_u32_e64 s[0:1], 1, v0
	s_nop 1
	v_writelane_b32 v254, s0, 13
	s_nop 1
	v_writelane_b32 v254, s1, 14
	s_cbranch_vccnz .LBB0_499
	s_mov_b32 s0, 0
	s_nop 0
	v_writelane_b32 v255, s0, 52
.Lk1_again:
	v_readlane_b32 s0, v251, 10
	v_readlane_b32 s2, v251, 12
	v_readlane_b32 s3, v251, 13
	v_mbcnt_lo_u32_b32 v0, -1, 0
	v_mbcnt_hi_u32_b32 v0, -1, v0
	s_mov_b64 s[16:17], s[2:3]
	v_add_u32_e32 v119, s95, v0
	v_readlane_b32 s1, v251, 11
	s_add_u32 s12, s16, 0x28600000
	s_addc_u32 s13, s17, 0
	v_readlane_b32 s0, v254, 13
	s_add_u32 s14, s16, 0x3a600000
	v_readlane_b32 s1, v254, 14
	s_addc_u32 s15, s17, 0
	v_and_b32_e32 v120, 63, v119
	v_and_b32_e32 v118, 15, v119
	v_readlane_b32 s2, v255, 52
	s_cmp_lg_u32 s2, 0
	s_cbranch_scc1 .Lk1_normal
	s_mov_b32 s2, 1
	s_nop 0
	v_writelane_b32 v255, s2, 52
	v_readfirstlane_b32 s0, v119
	s_branch .LBB0_432
.Lk1_normal:
	s_and_b64 vcc, exec, s[0:1]
	v_readfirstlane_b32 s0, v119
	s_cbranch_vccnz .LBB0_432
	s_add_u32 s18, s16, 0x3ae00000
	s_addc_u32 s19, s17, 0
	s_add_u32 s26, s16, 0x40e00000
	v_readlane_b32 s2, v254, 8
	v_readlane_b32 s36, v251, 14
	s_addc_u32 s27, s17, 0
	s_mov_b32 s4, s2
	s_mul_hi_u32 s1, s2, 0x18000
	s_mul_i32 s2, s2, 0x18000
	v_readlane_b32 s50, v251, 28
	v_readlane_b32 s37, v251, 15
	v_readlane_b32 s38, v251, 16
	v_readlane_b32 s39, v251, 17
	v_readlane_b32 s40, v251, 18
	v_readlane_b32 s41, v251, 19
	v_readlane_b32 s42, v251, 20
	v_readlane_b32 s43, v251, 21
	v_readlane_b32 s44, v251, 22
	v_readlane_b32 s45, v251, 23
	v_readlane_b32 s46, v251, 24
	v_readlane_b32 s47, v251, 25
	v_readlane_b32 s48, v251, 26
	v_readlane_b32 s49, v251, 27
	v_readlane_b32 s51, v251, 29
	s_add_u32 s20, s50, s2
	s_addc_u32 s21, s51, s1
	s_mul_i32 s2, s4, 0x6000
	v_readlane_b32 s36, v251, 32
	s_mul_hi_u32 s1, s4, 0x6000
	v_readlane_b32 s37, v251, 33
	s_add_u32 s22, s36, s2
	v_readlane_b32 s3, v254, 9
	s_addc_u32 s23, s37, s1
	s_lshl_b32 s86, s4, 6
	v_lshlrev_b32_e32 v2, 2, v120
	v_readlane_b32 s38, v251, 34
	s_lshl_b64 s[2:3], s[86:87], 2
	v_add_u32_e32 v3, 0xfc, v2
	v_readlane_b32 s39, v251, 35
	s_add_u32 s28, s38, s2
	v_and_b32_e32 v125, 0xfc, v3
	v_add_u32_e32 v3, 0xf8, v2
	v_readlane_b32 s40, v251, 36
	s_addc_u32 s29, s39, s3
	v_and_b32_e32 v126, 0xfc, v3
	v_add_u32_e32 v3, 0xf0, v2
	v_readlane_b32 s41, v251, 37
	s_add_u32 s30, s40, s2
	v_and_b32_e32 v127, 0xfc, v3
	v_add_u32_e32 v3, 0xe0, v2
	s_addc_u32 s31, s41, s3
	v_and_b32_e32 v128, 0xfc, v3
	v_add_u32_e32 v3, 0xc0, v2
	s_ashr_i32 s34, s0, 6
	s_and_b32 s0, s0, 0x3fffffc0
	v_lshrrev_b32_e32 v0, 4, v120
	v_mov_b32_e32 v1, 0x1000
	v_and_b32_e32 v129, 0xfc, v3
	v_lshrrev_b32_e32 v3, 2, v118
	s_lshl_b32 s0, s0, 2
	s_mul_i32 s1, s34, 0x2800
	v_lshl_or_b32 v121, v118, 3, v1
	v_and_b32_e32 v1, 7, v119
	v_lshl_or_b32 v3, v0, 2, v3
	v_lshlrev_b32_e32 v0, 1, v0
	s_add_i32 s0, s0, 0
	s_add_i32 s1, s1, 0
	s_add_i32 s35, s0, 0x1d800
	s_add_i32 s0, s0, 0x1d000
	v_lshl_or_b32 v131, s34, 3, v0
	v_mov_b32_e32 v0, s1
	v_lshl_add_u32 v8, v1, 4, s1
	s_movk_i32 s1, 0xa0
	v_and_b32_e32 v123, 56, v119
	v_xor_b32_e32 v130, 0x80, v2
	v_and_b32_e32 v4, 3, v119
	v_add_u32_e32 v132, s0, v2
	v_add_u32_e32 v133, s35, v2
	v_mad_u32_u24 v2, v3, s1, v0
	s_movk_i32 s1, 0x120
	v_and_b32_e32 v0, 48, v120
	v_and_b32_e32 v32, 48, v119
	v_readlane_b32 s42, v251, 38
	v_readlane_b32 s43, v251, 39
	v_readlane_b32 s44, v251, 40
	v_readlane_b32 s45, v251, 41
	v_readlane_b32 s46, v251, 42
	v_readlane_b32 s47, v251, 43
	v_lshlrev_b32_e32 v124, 3, v1
	s_waitcnt lgkmcnt(0)
	v_mul_u32_u24_e32 v5, 0x120, v3
	v_lshlrev_b32_e32 v6, 4, v4
	v_mul_u32_u24_e32 v7, 0xa0, v123
	v_lshlrev_b32_e32 v4, 3, v4
	v_mul_lo_u32 v134, v131, s1
	v_add_u32_e32 v135, s0, v0
	v_add_u32_e32 v136, s35, v0
	v_lshl_add_u64 v[0:1], s[16:17], 0, v[32:33]
	s_mov_b64 s[0:1], 0x41203040
	s_mov_b32 s79, 0x7ffff
	s_mov_b32 s78, 0x200000
	s_movk_i32 s77, 0x3000
	s_movk_i32 s76, 0x1000
	s_mov_b32 s75, 0x8000
	s_movk_i32 s74, 0x2000
	v_readlane_b32 s73, v254, 4
	v_readlane_b32 s71, v254, 3
	v_readlane_b32 s70, v254, 2
	v_readlane_b32 s72, v254, 1
	v_lshlrev_b32_e32 v122, 4, v118
	s_mov_b32 s33, 0
	v_cmp_eq_u32_e32 vcc, 0, v120
	v_cmp_gt_u32_e64 s[36:37], 2, v120
	v_cmp_gt_u32_e64 s[38:39], 4, v120
	v_cmp_gt_u32_e64 s[40:41], 8, v120
	v_cmp_gt_u32_e64 s[42:43], 16, v120
	v_cmp_gt_u32_e64 s[44:45], 32, v120
	v_add3_u32 v137, v5, v6, 0
	v_lshl_add_u64 v[86:87], v[0:1], 0, s[0:1]
	v_add_u32_e32 v138, v8, v7
	v_add_u32_e32 v139, v2, v4
	s_mov_b32 s46, s83
	s_mov_b32 s47, s83
	v_readlane_b32 s48, v251, 44
	v_readlane_b32 s49, v251, 45
	v_readlane_b32 s50, v251, 46
	v_readlane_b32 s51, v251, 47

.LBB0_432:
	v_readlane_b32 s0, v255, 52
	s_cmp_eq_u32 s0, 2
	s_cbranch_scc1 .LBB0_445
	v_readlane_b32 s0, v251, 54
	v_readlane_b32 s1, v251, 55
	s_andn2_b64 vcc, exec, s[0:1]
	v_readfirstlane_b32 s0, v119
	s_waitcnt lgkmcnt(0)
	s_barrier
	s_cbranch_vccnz .LBB0_445
	v_add_u32_e32 v4, 0x200, v119
	s_ashr_i32 s8, s0, 6
	v_bfe_u32 v1, v119, 4, 2
	s_movk_i32 s1, 0x410
	v_ashrrev_i32_e32 v90, 6, v119
	v_ashrrev_i32_e32 v91, 6, v4
	s_add_u32 s0, s16, 0x55200000
	v_lshlrev_b32_e32 v86, 3, v1
	v_mad_u32_u24 v3, v118, s1, 0
	v_lshlrev_b32_e32 v87, 4, v1
	v_mul_lo_u32 v1, v90, s1
	v_mul_lo_u32 v4, v91, s1
	s_addc_u32 s1, s17, 0
	s_add_u32 s2, s16, 0x75b00000
	v_lshlrev_b32_e32 v0, 3, v120
	v_lshl_add_u32 v2, v120, 4, 0
	s_addc_u32 s3, s17, 0
	s_lshl_b32 s9, s8, 11
	s_or_b32 s10, s9, 64
	s_lshl_b32 s11, s8, 4
	v_lshlrev_b32_e32 v32, 1, v0
	v_add_u32_e32 v92, v2, v1
	v_add_u32_e32 v93, v2, v4
	v_add_u32_e32 v94, v3, v87
	s_mov_b32 s16, s83
	s_branch .LBB0_435

.LBB0_445:
	v_readlane_b32 s0, v255, 52
	s_cmp_eq_u32 s0, 1
	s_cbranch_scc0 .Lk1_done
	s_mov_b32 s0, 2
	s_nop 0
	v_writelane_b32 v255, s0, 52
	s_waitcnt lgkmcnt(0)
	s_barrier
	s_branch .Lk1_again
